# MoE down epilogue: one load wait per row half; the per-row-group blocks no longer drain the previous block's stores
# baseline (speedup 1.0000x reference)
.LBB0_1616:
	v_lshl_add_u32 v174, s55, 10, v189
	ds_read2_b32 v[128:129], v174 offset1:16
	ds_read2_b32 v[130:131], v174 offset0:32 offset1:48
	v_or_b32_e32 v172, s17, v190
	v_ashrrev_i32_e32 v173, 31, v172
	v_lshl_add_u64 v[178:179], v[172:173], 1, s[10:11]
	s_waitcnt lgkmcnt(0)
	v_ashrrev_i32_e32 v187, 31, v128
	v_mov_b32_e32 v186, v128
	v_ashrrev_i32_e32 v185, 31, v129
	v_mov_b32_e32 v184, v129
	v_lshlrev_b64 v[128:129], 10, v[186:187]
	v_cmp_lt_i64_e32 vcc, -1, v[186:187]
	v_cmp_lt_i64_e64 s[4:5], -1, v[184:185]
	v_ashrrev_i32_e32 v183, 31, v130
	v_cndmask_b32_e32 v129, 0, v129, vcc
	v_cndmask_b32_e32 v128, 0, v128, vcc
	v_lshl_add_u64 v[128:129], v[128:129], 1, v[178:179]
	global_load_dwordx4 v[156:159], v[128:129], off
	global_load_dwordx4 v[152:155], v[128:129], off offset:64
	v_lshlrev_b64 v[128:129], 10, v[184:185]
	v_cndmask_b32_e64 v129, 0, v129, s[4:5]
	v_cndmask_b32_e64 v128, 0, v128, s[4:5]
	v_mov_b32_e32 v182, v130
	v_lshl_add_u64 v[128:129], v[128:129], 1, v[178:179]
	global_load_dwordx4 v[148:151], v[128:129], off
	global_load_dwordx4 v[144:147], v[128:129], off offset:64
	v_lshlrev_b64 v[128:129], 10, v[182:183]
	v_cmp_lt_i64_e64 s[4:5], -1, v[182:183]
	v_ashrrev_i32_e32 v181, 31, v131
	v_mov_b32_e32 v180, v131
	v_cndmask_b32_e64 v129, 0, v129, s[4:5]
	v_cndmask_b32_e64 v128, 0, v128, s[4:5]
	v_lshl_add_u64 v[128:129], v[128:129], 1, v[178:179]
	global_load_dwordx4 v[140:143], v[128:129], off
	global_load_dwordx4 v[136:139], v[128:129], off offset:64
	v_lshlrev_b64 v[128:129], 10, v[180:181]
	v_cmp_lt_i64_e64 s[4:5], -1, v[180:181]
	s_nop 1
	v_cndmask_b32_e64 v129, 0, v129, s[4:5]
	v_cndmask_b32_e64 v128, 0, v128, s[4:5]
	v_lshl_add_u64 v[128:129], v[128:129], 1, v[178:179]
	global_load_dwordx4 v[132:135], v[128:129], off
	s_nop 0
	global_load_dwordx4 v[128:131], v[128:129], off offset:64
	ds_read2_b32 v[176:177], v174 offset0:128 offset1:144
	ds_read2_b32 v[174:175], v174 offset0:160 offset1:176
	s_waitcnt vmcnt(0)
	s_and_saveexec_b64 s[4:5], vcc
	s_cbranch_execnz .LBB0_1629
	s_or_b64 exec, exec, s[4:5]
	v_cmp_lt_i32_e32 vcc, -1, v184
	s_and_saveexec_b64 s[4:5], vcc
	s_cbranch_execnz .LBB0_1630

.LBB0_1620:
	v_lshlrev_b32_e32 v82, 16, v132
	v_and_b32_e32 v83, 0xffff0000, v132
	v_pk_add_f32 v[76:77], v[76:77], v[82:83]
	v_lshlrev_b32_e32 v82, 16, v133
	v_and_b32_e32 v83, 0xffff0000, v133
	v_pk_add_f32 v[78:79], v[78:79], v[82:83]
	v_cvt_pk_bf16_f32 v76, v76, v77
	v_cvt_pk_bf16_f32 v77, v78, v79
	v_lshlrev_b32_e32 v78, 16, v134
	v_and_b32_e32 v79, 0xffff0000, v134
	v_pk_add_f32 v[72:73], v[72:73], v[78:79]
	v_lshlrev_b64 v[80:81], 11, v[180:181]
	v_cvt_pk_bf16_f32 v78, v72, v73
	v_lshlrev_b32_e32 v72, 16, v135
	v_and_b32_e32 v73, 0xffff0000, v135
	v_pk_add_f32 v[72:73], v[74:75], v[72:73]
	v_lshlrev_b32_e32 v74, 16, v128
	v_and_b32_e32 v75, 0xffff0000, v128
	v_pk_add_f32 v[68:69], v[68:69], v[74:75]
	v_lshlrev_b32_e32 v74, 16, v129
	v_and_b32_e32 v75, 0xffff0000, v129
	v_pk_add_f32 v[70:71], v[70:71], v[74:75]
	v_cvt_pk_bf16_f32 v68, v68, v69
	v_cvt_pk_bf16_f32 v69, v70, v71
	v_lshlrev_b32_e32 v70, 16, v130
	v_and_b32_e32 v71, 0xffff0000, v130
	v_pk_add_f32 v[64:65], v[64:65], v[70:71]
	v_cvt_pk_bf16_f32 v79, v72, v73
	v_cvt_pk_bf16_f32 v70, v64, v65
	v_lshlrev_b32_e32 v64, 16, v131
	v_and_b32_e32 v65, 0xffff0000, v131
	v_lshl_add_u64 v[72:73], s[10:11], 0, v[80:81]
	v_pk_add_f32 v[64:65], v[66:67], v[64:65]
	v_lshl_add_u64 v[72:73], v[172:173], 1, v[72:73]
	v_cvt_pk_bf16_f32 v71, v64, v65
	global_store_dwordx4 v[72:73], v[76:79], off
	global_store_dwordx4 v[72:73], v[68:71], off offset:64
.LBB0_1621:
	s_or_b64 exec, exec, s[4:5]
	s_waitcnt lgkmcnt(0)
	v_mov_b32_e32 v208, v176
	v_lshlrev_b64 v[64:65], 10, v[208:209]
	v_cmp_lt_i32_e32 vcc, -1, v176
	v_mov_b32_e32 v100, v177
	v_mov_b32_e32 v101, v209
	v_cndmask_b32_e32 v65, 0, v65, vcc
	v_cndmask_b32_e32 v64, 0, v64, vcc
	v_lshl_add_u64 v[64:65], v[64:65], 1, v[178:179]
	global_load_dwordx4 v[92:95], v[64:65], off
	global_load_dwordx4 v[88:91], v[64:65], off offset:64
	v_lshlrev_b64 v[64:65], 10, v[100:101]
	v_cmp_lt_i32_e64 s[4:5], -1, v177
	v_mov_b32_e32 v98, v174
	v_mov_b32_e32 v99, v209
	v_cndmask_b32_e64 v65, 0, v65, s[4:5]
	v_cndmask_b32_e64 v64, 0, v64, s[4:5]
	v_lshl_add_u64 v[64:65], v[64:65], 1, v[178:179]
	global_load_dwordx4 v[84:87], v[64:65], off
	global_load_dwordx4 v[80:83], v[64:65], off offset:64
	v_lshlrev_b64 v[64:65], 10, v[98:99]
	v_cmp_lt_i32_e64 s[4:5], -1, v174
	v_mov_b32_e32 v96, v175
	v_mov_b32_e32 v97, v209
	v_cndmask_b32_e64 v65, 0, v65, s[4:5]
	v_cndmask_b32_e64 v64, 0, v64, s[4:5]
	v_lshl_add_u64 v[64:65], v[64:65], 1, v[178:179]
	global_load_dwordx4 v[76:79], v[64:65], off
	global_load_dwordx4 v[72:75], v[64:65], off offset:64
	v_lshlrev_b64 v[64:65], 10, v[96:97]
	v_cmp_lt_i32_e64 s[4:5], -1, v175
	s_nop 1
	v_cndmask_b32_e64 v65, 0, v65, s[4:5]
	v_cndmask_b32_e64 v64, 0, v64, s[4:5]
	v_lshl_add_u64 v[64:65], v[64:65], 1, v[178:179]
	global_load_dwordx4 v[68:71], v[64:65], off
	s_nop 0
	global_load_dwordx4 v[64:67], v[64:65], off offset:64
	s_waitcnt vmcnt(0)
	s_and_saveexec_b64 s[4:5], vcc
	s_cbranch_execnz .LBB0_1632
	s_or_b64 exec, exec, s[4:5]
	v_cmp_lt_i32_e32 vcc, -1, v177
	s_and_saveexec_b64 s[4:5], vcc
	s_cbranch_execnz .LBB0_1633

.LBB0_1625:
	v_lshlrev_b32_e32 v10, 16, v68
	v_and_b32_e32 v11, 0xffff0000, v68
	v_pk_add_f32 v[4:5], v[4:5], v[10:11]
	v_lshlrev_b32_e32 v10, 16, v69
	v_and_b32_e32 v11, 0xffff0000, v69
	v_pk_add_f32 v[6:7], v[6:7], v[10:11]
	v_cvt_pk_bf16_f32 v4, v4, v5
	v_cvt_pk_bf16_f32 v5, v6, v7
	v_lshlrev_b32_e32 v6, 16, v70
	v_and_b32_e32 v7, 0xffff0000, v70
	v_pk_add_f32 v[0:1], v[0:1], v[6:7]
	v_lshlrev_b64 v[8:9], 11, v[96:97]
	v_cvt_pk_bf16_f32 v6, v0, v1
	v_lshlrev_b32_e32 v0, 16, v71
	v_and_b32_e32 v1, 0xffff0000, v71
	v_pk_add_f32 v[0:1], v[2:3], v[0:1]
	v_lshlrev_b32_e32 v2, 16, v65
	v_cvt_pk_bf16_f32 v7, v0, v1
	v_lshl_add_u64 v[0:1], s[10:11], 0, v[8:9]
	v_lshl_add_u64 v[8:9], v[172:173], 1, v[0:1]
	v_lshlrev_b32_e32 v0, 16, v64
	v_and_b32_e32 v1, 0xffff0000, v64
	v_and_b32_e32 v3, 0xffff0000, v65
	v_pk_add_f32 v[0:1], v[16:17], v[0:1]
	v_pk_add_f32 v[2:3], v[18:19], v[2:3]
	global_store_dwordx4 v[8:9], v[4:7], off
	v_cvt_pk_bf16_f32 v0, v0, v1
	v_cvt_pk_bf16_f32 v1, v2, v3
	v_lshlrev_b32_e32 v2, 16, v66
	v_and_b32_e32 v3, 0xffff0000, v66
	v_lshlrev_b32_e32 v4, 16, v67
	v_and_b32_e32 v5, 0xffff0000, v67
	v_pk_add_f32 v[2:3], v[12:13], v[2:3]
	v_pk_add_f32 v[4:5], v[14:15], v[4:5]
	v_cvt_pk_bf16_f32 v2, v2, v3
	v_cvt_pk_bf16_f32 v3, v4, v5
	global_store_dwordx4 v[8:9], v[0:3], off offset:64

.LBB0_1629:
	v_lshlrev_b32_e32 v192, 16, v156
	v_and_b32_e32 v193, 0xffff0000, v156
	v_lshlrev_b32_e32 v156, 16, v157
	v_and_b32_e32 v157, 0xffff0000, v157
	v_pk_add_f32 v[124:125], v[124:125], v[192:193]
	v_pk_add_f32 v[126:127], v[126:127], v[156:157]
	v_cvt_pk_bf16_f32 v124, v124, v125
	v_cvt_pk_bf16_f32 v125, v126, v127
	v_lshlrev_b32_e32 v126, 16, v158
	v_and_b32_e32 v127, 0xffff0000, v158
	v_pk_add_f32 v[120:121], v[120:121], v[126:127]
	v_lshlrev_b64 v[186:187], 11, v[186:187]
	v_cvt_pk_bf16_f32 v126, v120, v121
	v_lshlrev_b32_e32 v120, 16, v159
	v_and_b32_e32 v121, 0xffff0000, v159
	v_pk_add_f32 v[120:121], v[122:123], v[120:121]
	v_lshlrev_b32_e32 v122, 16, v152
	v_and_b32_e32 v123, 0xffff0000, v152
	v_pk_add_f32 v[116:117], v[116:117], v[122:123]
	v_lshlrev_b32_e32 v122, 16, v153
	v_and_b32_e32 v123, 0xffff0000, v153
	v_pk_add_f32 v[118:119], v[118:119], v[122:123]
	v_cvt_pk_bf16_f32 v116, v116, v117
	v_cvt_pk_bf16_f32 v117, v118, v119
	v_lshlrev_b32_e32 v118, 16, v154
	v_and_b32_e32 v119, 0xffff0000, v154
	v_pk_add_f32 v[112:113], v[112:113], v[118:119]
	v_cvt_pk_bf16_f32 v127, v120, v121
	v_cvt_pk_bf16_f32 v118, v112, v113
	v_lshlrev_b32_e32 v112, 16, v155
	v_and_b32_e32 v113, 0xffff0000, v155
	v_lshl_add_u64 v[120:121], s[10:11], 0, v[186:187]
	v_pk_add_f32 v[112:113], v[114:115], v[112:113]
	v_lshl_add_u64 v[120:121], v[172:173], 1, v[120:121]
	v_cvt_pk_bf16_f32 v119, v112, v113
	global_store_dwordx4 v[120:121], v[124:127], off
	global_store_dwordx4 v[120:121], v[116:119], off offset:64
	s_or_b64 exec, exec, s[4:5]
	v_cmp_lt_i32_e32 vcc, -1, v184
	s_and_saveexec_b64 s[4:5], vcc
	s_cbranch_execz .LBB0_1618
.LBB0_1630:
	v_lshlrev_b32_e32 v114, 16, v148
	v_and_b32_e32 v115, 0xffff0000, v148
	v_pk_add_f32 v[108:109], v[108:109], v[114:115]
	v_lshlrev_b32_e32 v114, 16, v149
	v_and_b32_e32 v115, 0xffff0000, v149
	v_pk_add_f32 v[110:111], v[110:111], v[114:115]
	v_cvt_pk_bf16_f32 v108, v108, v109
	v_cvt_pk_bf16_f32 v109, v110, v111
	v_lshlrev_b32_e32 v110, 16, v150
	v_and_b32_e32 v111, 0xffff0000, v150
	v_pk_add_f32 v[104:105], v[104:105], v[110:111]
	v_lshlrev_b64 v[112:113], 11, v[184:185]
	v_cvt_pk_bf16_f32 v110, v104, v105
	v_lshlrev_b32_e32 v104, 16, v151
	v_and_b32_e32 v105, 0xffff0000, v151
	v_pk_add_f32 v[104:105], v[106:107], v[104:105]
	v_lshlrev_b32_e32 v106, 16, v144
	v_and_b32_e32 v107, 0xffff0000, v144
	v_pk_add_f32 v[100:101], v[100:101], v[106:107]
	v_lshlrev_b32_e32 v106, 16, v145
	v_and_b32_e32 v107, 0xffff0000, v145
	v_pk_add_f32 v[102:103], v[102:103], v[106:107]
	v_cvt_pk_bf16_f32 v100, v100, v101
	v_cvt_pk_bf16_f32 v101, v102, v103
	v_lshlrev_b32_e32 v102, 16, v146
	v_and_b32_e32 v103, 0xffff0000, v146
	v_pk_add_f32 v[96:97], v[96:97], v[102:103]
	v_cvt_pk_bf16_f32 v111, v104, v105
	v_cvt_pk_bf16_f32 v102, v96, v97
	v_lshlrev_b32_e32 v96, 16, v147
	v_and_b32_e32 v97, 0xffff0000, v147
	v_lshl_add_u64 v[104:105], s[10:11], 0, v[112:113]
	v_pk_add_f32 v[96:97], v[98:99], v[96:97]
	v_lshl_add_u64 v[104:105], v[172:173], 1, v[104:105]
	v_cvt_pk_bf16_f32 v103, v96, v97
	global_store_dwordx4 v[104:105], v[108:111], off
	global_store_dwordx4 v[104:105], v[100:103], off offset:64
	s_or_b64 exec, exec, s[4:5]
	v_cmp_lt_i32_e32 vcc, -1, v182
	s_and_saveexec_b64 s[4:5], vcc
	s_cbranch_execz .LBB0_1619
.LBB0_1631:
	v_lshlrev_b32_e32 v98, 16, v140
	v_and_b32_e32 v99, 0xffff0000, v140
	v_pk_add_f32 v[92:93], v[92:93], v[98:99]
	v_lshlrev_b32_e32 v98, 16, v141
	v_and_b32_e32 v99, 0xffff0000, v141
	v_pk_add_f32 v[94:95], v[94:95], v[98:99]
	v_cvt_pk_bf16_f32 v92, v92, v93
	v_cvt_pk_bf16_f32 v93, v94, v95
	v_lshlrev_b32_e32 v94, 16, v142
	v_and_b32_e32 v95, 0xffff0000, v142
	v_pk_add_f32 v[88:89], v[88:89], v[94:95]
	v_lshlrev_b64 v[96:97], 11, v[182:183]
	v_cvt_pk_bf16_f32 v94, v88, v89
	v_lshlrev_b32_e32 v88, 16, v143
	v_and_b32_e32 v89, 0xffff0000, v143
	v_pk_add_f32 v[88:89], v[90:91], v[88:89]
	v_lshlrev_b32_e32 v90, 16, v136
	v_and_b32_e32 v91, 0xffff0000, v136
	v_pk_add_f32 v[84:85], v[84:85], v[90:91]
	v_lshlrev_b32_e32 v90, 16, v137
	v_and_b32_e32 v91, 0xffff0000, v137
	v_pk_add_f32 v[86:87], v[86:87], v[90:91]
	v_cvt_pk_bf16_f32 v84, v84, v85
	v_cvt_pk_bf16_f32 v85, v86, v87
	v_lshlrev_b32_e32 v86, 16, v138
	v_and_b32_e32 v87, 0xffff0000, v138
	v_pk_add_f32 v[80:81], v[80:81], v[86:87]
	v_cvt_pk_bf16_f32 v95, v88, v89
	v_cvt_pk_bf16_f32 v86, v80, v81
	v_lshlrev_b32_e32 v80, 16, v139
	v_and_b32_e32 v81, 0xffff0000, v139
	v_lshl_add_u64 v[88:89], s[10:11], 0, v[96:97]
	v_pk_add_f32 v[80:81], v[82:83], v[80:81]
	v_lshl_add_u64 v[88:89], v[172:173], 1, v[88:89]
	v_cvt_pk_bf16_f32 v87, v80, v81
	global_store_dwordx4 v[88:89], v[92:95], off
	global_store_dwordx4 v[88:89], v[84:87], off offset:64
	s_or_b64 exec, exec, s[4:5]
	v_cmp_lt_i32_e32 vcc, -1, v180
	s_and_saveexec_b64 s[4:5], vcc
	s_cbranch_execnz .LBB0_1620
	s_branch .LBB0_1621
.LBB0_1632:
	v_lshlrev_b32_e32 v104, 16, v92
	v_and_b32_e32 v105, 0xffff0000, v92
	v_lshlrev_b32_e32 v92, 16, v93
	v_and_b32_e32 v93, 0xffff0000, v93
	v_pk_add_f32 v[52:53], v[52:53], v[104:105]
	v_pk_add_f32 v[54:55], v[54:55], v[92:93]
	v_cvt_pk_bf16_f32 v52, v52, v53
	v_cvt_pk_bf16_f32 v53, v54, v55
	v_lshlrev_b32_e32 v54, 16, v94
	v_and_b32_e32 v55, 0xffff0000, v94
	v_pk_add_f32 v[48:49], v[48:49], v[54:55]
	v_lshlrev_b64 v[102:103], 11, v[208:209]
	v_cvt_pk_bf16_f32 v54, v48, v49
	v_lshlrev_b32_e32 v48, 16, v95
	v_and_b32_e32 v49, 0xffff0000, v95
	v_pk_add_f32 v[48:49], v[50:51], v[48:49]
	v_lshlrev_b32_e32 v50, 16, v89
	v_cvt_pk_bf16_f32 v55, v48, v49
	v_lshl_add_u64 v[48:49], s[10:11], 0, v[102:103]
	v_lshl_add_u64 v[92:93], v[172:173], 1, v[48:49]
	v_lshlrev_b32_e32 v48, 16, v88
	v_and_b32_e32 v49, 0xffff0000, v88
	v_and_b32_e32 v51, 0xffff0000, v89
	v_pk_add_f32 v[48:49], v[60:61], v[48:49]
	v_pk_add_f32 v[50:51], v[62:63], v[50:51]
	global_store_dwordx4 v[92:93], v[52:55], off
	v_cvt_pk_bf16_f32 v48, v48, v49
	v_cvt_pk_bf16_f32 v49, v50, v51
	v_lshlrev_b32_e32 v50, 16, v90
	v_and_b32_e32 v51, 0xffff0000, v90
	v_lshlrev_b32_e32 v52, 16, v91
	v_and_b32_e32 v53, 0xffff0000, v91
	v_pk_add_f32 v[50:51], v[56:57], v[50:51]
	v_pk_add_f32 v[52:53], v[58:59], v[52:53]
	v_cvt_pk_bf16_f32 v50, v50, v51
	v_cvt_pk_bf16_f32 v51, v52, v53
	global_store_dwordx4 v[92:93], v[48:51], off offset:64
	s_or_b64 exec, exec, s[4:5]
	v_cmp_lt_i32_e32 vcc, -1, v177
	s_and_saveexec_b64 s[4:5], vcc
	s_cbranch_execz .LBB0_1623
.LBB0_1633:
	v_lshlrev_b32_e32 v50, 16, v84
	v_and_b32_e32 v51, 0xffff0000, v84
	v_pk_add_f32 v[36:37], v[36:37], v[50:51]
	v_lshlrev_b32_e32 v50, 16, v85
	v_and_b32_e32 v51, 0xffff0000, v85
	v_pk_add_f32 v[38:39], v[38:39], v[50:51]
	v_cvt_pk_bf16_f32 v36, v36, v37
	v_cvt_pk_bf16_f32 v37, v38, v39
	v_lshlrev_b32_e32 v38, 16, v86
	v_and_b32_e32 v39, 0xffff0000, v86
	v_pk_add_f32 v[32:33], v[32:33], v[38:39]
	v_lshlrev_b64 v[48:49], 11, v[100:101]
	v_cvt_pk_bf16_f32 v38, v32, v33
	v_lshlrev_b32_e32 v32, 16, v87
	v_and_b32_e32 v33, 0xffff0000, v87
	v_pk_add_f32 v[32:33], v[34:35], v[32:33]
	v_lshlrev_b32_e32 v34, 16, v81
	v_cvt_pk_bf16_f32 v39, v32, v33
	v_lshl_add_u64 v[32:33], s[10:11], 0, v[48:49]
	v_lshl_add_u64 v[48:49], v[172:173], 1, v[32:33]
	v_lshlrev_b32_e32 v32, 16, v80
	v_and_b32_e32 v33, 0xffff0000, v80
	v_and_b32_e32 v35, 0xffff0000, v81
	v_pk_add_f32 v[32:33], v[44:45], v[32:33]
	v_pk_add_f32 v[34:35], v[46:47], v[34:35]
	global_store_dwordx4 v[48:49], v[36:39], off
	v_cvt_pk_bf16_f32 v32, v32, v33
	v_cvt_pk_bf16_f32 v33, v34, v35
	v_lshlrev_b32_e32 v34, 16, v82
	v_and_b32_e32 v35, 0xffff0000, v82
	v_lshlrev_b32_e32 v36, 16, v83
	v_and_b32_e32 v37, 0xffff0000, v83
	v_pk_add_f32 v[34:35], v[40:41], v[34:35]
	v_pk_add_f32 v[36:37], v[42:43], v[36:37]
	v_cvt_pk_bf16_f32 v34, v34, v35
	v_cvt_pk_bf16_f32 v35, v36, v37
	global_store_dwordx4 v[48:49], v[32:35], off offset:64
	s_or_b64 exec, exec, s[4:5]
	v_cmp_lt_i32_e32 vcc, -1, v174
	s_and_saveexec_b64 s[4:5], vcc
	s_cbranch_execz .LBB0_1624
.LBB0_1634:
	v_lshlrev_b32_e32 v34, 16, v76
	v_and_b32_e32 v35, 0xffff0000, v76
	v_pk_add_f32 v[20:21], v[20:21], v[34:35]
	v_lshlrev_b32_e32 v34, 16, v77
	v_and_b32_e32 v35, 0xffff0000, v77
	v_pk_add_f32 v[22:23], v[22:23], v[34:35]
	v_cvt_pk_bf16_f32 v20, v20, v21
	v_cvt_pk_bf16_f32 v21, v22, v23
	v_lshlrev_b32_e32 v22, 16, v78
	v_and_b32_e32 v23, 0xffff0000, v78
	v_pk_add_f32 v[8:9], v[8:9], v[22:23]
	v_lshlrev_b64 v[32:33], 11, v[98:99]
	v_cvt_pk_bf16_f32 v22, v8, v9
	v_lshlrev_b32_e32 v8, 16, v79
	v_and_b32_e32 v9, 0xffff0000, v79
	v_pk_add_f32 v[8:9], v[10:11], v[8:9]
	v_lshlrev_b32_e32 v10, 16, v73
	v_cvt_pk_bf16_f32 v23, v8, v9
	v_lshl_add_u64 v[8:9], s[10:11], 0, v[32:33]
	v_lshl_add_u64 v[32:33], v[172:173], 1, v[8:9]
	v_lshlrev_b32_e32 v8, 16, v72
	v_and_b32_e32 v9, 0xffff0000, v72
	v_and_b32_e32 v11, 0xffff0000, v73
	v_pk_add_f32 v[8:9], v[28:29], v[8:9]
	v_pk_add_f32 v[10:11], v[30:31], v[10:11]
	global_store_dwordx4 v[32:33], v[20:23], off
	v_cvt_pk_bf16_f32 v8, v8, v9
	v_cvt_pk_bf16_f32 v9, v10, v11
	v_lshlrev_b32_e32 v10, 16, v74
	v_and_b32_e32 v11, 0xffff0000, v74
	v_lshlrev_b32_e32 v20, 16, v75
	v_and_b32_e32 v21, 0xffff0000, v75
	v_pk_add_f32 v[10:11], v[24:25], v[10:11]
	v_pk_add_f32 v[20:21], v[26:27], v[20:21]
	v_cvt_pk_bf16_f32 v10, v10, v11
	v_cvt_pk_bf16_f32 v11, v20, v21
	global_store_dwordx4 v[32:33], v[8:11], off offset:64
	s_or_b64 exec, exec, s[4:5]
	v_cmp_lt_i32_e32 vcc, -1, v175
	s_and_saveexec_b64 s[4:5], vcc
	s_cbranch_execnz .LBB0_1625
	s_branch .LBB0_1626
